# v66 + every 16th arriver of an XCD starts an asynchronous L2 write-back while it waits at the grid barrier
# baseline (speedup 1.0000x reference)
; __device__ __forceinline__ unsigned xb_ld(unsigned* p)              { return __hip_atomic_load(p, __ATOMIC_RELAXED, __HIP_MEMORY_SCOPE_AGENT); }
; __device__ __forceinline__ unsigned xb_add(unsigned* p, unsigned v) { return __hip_atomic_fetch_add(p, v, __ATOMIC_RELAXED, __HIP_MEMORY_SCOPE_AGENT); }
; #define XB_SPIN(cond, bar) do { unsigned _sp = 0; while (cond) { __builtin_amdgcn_s_sleep(1); \
;     if ((++_sp & 255u) == 0u) { if (xb_ld(&(bar)[XB_TMO])) break; if (_sp > XB_SPIN_CAP) { atomicAdd(&(bar)[XB_TMO], 1u); break; } } } } while (0)
; __device__ __forceinline__ void xcd_barrier(const XcdBarrier& b) {
;     ...
;         const unsigned old = xb_add(&bar[XB_XSUB(b.x)], 1u);
;         const unsigned gen = old / nloc;
;         if (old + 1u == (gen + 1u) * nloc) {
;             __builtin_amdgcn_fence(__ATOMIC_RELEASE, "agent");
;             asm volatile("s_waitcnt vmcnt(0)" ::: "memory");
;             const unsigned og = xb_add(&bar[XB_TOP], 1u);
;             const unsigned tg = og / nx;
;             if (og + 1u == (tg + 1u) * nx) xb_add(&bar[XB_TOPGEN], 1u);
;             else XB_SPIN(xb_ld(&bar[XB_TOPGEN]) == tg, bar);
;             __builtin_amdgcn_fence(__ATOMIC_ACQUIRE, "agent");
;             xb_add(&bar[XB_XGEN(b.x)], 1u);
;             asm volatile("s_waitcnt vmcnt(0)" ::: "memory");
;         } else {
;             XB_SPIN(xb_ld(&bar[XB_XGEN(b.x)]) == gen, bar);
.LBB0_162:
	s_lshl_b32 s0, s54, 8
	s_add_u32 s25, s55, s0
	s_addc_u32 s24, s56, 0
	v_mov_b32_e32 v3, s25
	v_add_co_u32_e32 v6, vcc, 0x1000, v3
	v_mov_b32_e32 v3, s24
	s_nop 0
	v_addc_co_u32_e32 v7, vcc, 0, v3, vcc
	v_mov_b32_e32 v3, 1
	flat_atomic_add v3, v[6:7], v3 offset:1024 sc0
	v_cvt_f32_u32_e32 v5, v4
	v_sub_u32_e32 v6, 0, v4
	v_rcp_iflag_f32_e32 v5, v5
	s_nop 0
	v_mul_f32_e32 v5, 0x4f7ffffe, v5
	v_cvt_u32_f32_e32 v5, v5
	v_mul_lo_u32 v6, v6, v5
	v_mul_hi_u32 v6, v5, v6
	v_add_u32_e32 v5, v5, v6
	s_waitcnt vmcnt(0) lgkmcnt(0)
	v_mul_hi_u32 v5, v3, v5
	v_mul_lo_u32 v7, v5, v4
	v_add_u32_e32 v6, 1, v3
	v_sub_u32_e32 v3, v3, v7
	v_add_u32_e32 v8, 1, v5
	v_cmp_ge_u32_e32 vcc, v3, v4
	v_sub_u32_e32 v7, v3, v4
	s_nop 0
	v_cndmask_b32_e32 v5, v5, v8, vcc
	v_cndmask_b32_e32 v3, v3, v7, vcc
	v_add_u32_e32 v7, 1, v5
	v_cmp_ge_u32_e32 vcc, v3, v4
	s_nop 1
	v_cndmask_b32_e32 v3, v5, v7, vcc
	v_mad_u64_u32 v[4:5], s[0:1], v4, v3, v[4:5]
	v_cmp_ne_u32_e32 vcc, v6, v4
	s_and_saveexec_b64 s[0:1], vcc
	s_xor_b64 s[0:1], exec, s[0:1]
	s_cbranch_execz .LBB0_175
	v_and_b32_e32 v2, 15, v6
	v_cmp_eq_u32_e32 vcc, 0, v2
	s_cbranch_vccz .Lbwb_0
	buffer_wbl2 sc1
.Lbwb_0:
	v_mov_b32_e32 v2, s25
	v_add_co_u32_e32 v4, vcc, 0x2000, v2
	v_mov_b32_e32 v2, s24
	s_nop 0
	v_addc_co_u32_e32 v5, vcc, 0, v2, vcc
	s_add_u32 s8, s36, 0x7500
	s_addc_u32 s9, s37, 0
	v_mov_b64_e32 v[4:5], s[8:9]
	buffer_inv sc1
	flat_load_dword v2, v[4:5] sc1
	s_waitcnt vmcnt(0) lgkmcnt(0)
	v_cmp_eq_u32_e32 vcc, v2, v3
	s_and_saveexec_b64 s[4:5], vcc
	s_cbranch_execz .LBB0_174
	s_add_u32 s6, s36, 0x4200
	s_addc_u32 s7, s37, 0
	s_mov_b32 s26, 1
	s_mov_b64 s[10:11], 0
	s_branch .LBB0_166
